# speedup vs baseline: 1.0023x; 1.0010x over previous
_Z12scan2_kernelPKDF16_S0_S0_S0_S0_PKfS2_S2_S2_PDF16_PfS4_:
	s_and_b32 s3, s2, 7
	s_lshr_b32 s2, s2, 3
	s_lshl_b32 s3, s3, 5
	s_or_b32 s2, s2, s3
	s_load_dwordx8 s[4:11], s[0:1], 0x0
	s_load_dwordx8 s[12:19], s[0:1], 0x20
	s_load_dwordx4 s[20:23], s[0:1], 0x40
	s_load_dwordx2 s[24:25], s[0:1], 0x50
	s_and_b32 s26, s2, 3
	s_bfe_u32 s27, s2, 0x50002
	s_lshr_b32 s28, s2, 7
	s_lshl_b32 s29, s26, 3
	v_lshrrev_b32_e32 v1, 6, v0
	v_and_b32_e32 v2, 15, v0
	v_bfe_u32 v3, v0, 4, 2
	v_and_b32_e32 v42, 63, v0
	v_readfirstlane_b32 s40, v1
	v_mov_b32_e32 v43, v0
	v_lshrrev_b32_e32 v14, 4, v43
	v_and_b32_e32 v15, 15, v43
	v_and_b32_e32 v188, 15, v14
	v_xor_b32_e32 v15, v15, v188
	v_lshlrev_b32_e32 v15, 4, v15
	v_lshl_or_b32 v4, v14, 13, v15
	v_lshl_or_b32 v6, v14, 8, v15
	v_lshrrev_b32_e32 v14, 3, v43
	v_and_b32_e32 v15, 7, v43
	v_and_b32_e32 v188, 7, v14
	v_xor_b32_e32 v15, v15, v188
	v_lshlrev_b32_e32 v15, 4, v15
	v_lshl_or_b32 v8, v14, 12, v15
	v_lshlrev_b32_e32 v40, 4, v43
	v_add_u32_e32 v32, 0xc800, v40
	v_add_u32_e32 v43, 0x200, v0
	v_lshrrev_b32_e32 v14, 4, v43
	v_and_b32_e32 v15, 15, v43
	v_and_b32_e32 v188, 15, v14
	v_xor_b32_e32 v15, v15, v188
	v_lshlrev_b32_e32 v15, 4, v15
	v_lshl_or_b32 v5, v14, 13, v15
	v_lshl_or_b32 v7, v14, 8, v15
	v_lshrrev_b32_e32 v14, 3, v43
	v_and_b32_e32 v15, 7, v43
	v_and_b32_e32 v188, 7, v14
	v_xor_b32_e32 v15, v15, v188
	v_lshlrev_b32_e32 v15, 4, v15
	v_lshl_or_b32 v9, v14, 12, v15
	v_lshlrev_b32_e32 v41, 4, v43
	v_add_u32_e32 v33, 0xc800, v41
	s_sub_u32 s45, 11, s40
	s_cmp_lt_u32 s40, 4
	s_cselect_b32 s41, s40, s45
	s_lshr_b32 s42, s41, 1
	s_lshl_b32 s43, s40, 10
	s_lshl_b32 s44, s40, 8
	s_and_b32 s45, s40, 1
	s_lshl_b32 s45, s45, 8
	v_lshl_add_u32 v10, v42, 2, s45
	s_lshl_b32 s45, s41, 4
	v_add_u32_e32 v14, s45, v2
	v_add_u32_e32 v15, 0, v3
	v_xor_b32_e32 v15, v15, v2
	v_lshlrev_b32_e32 v15, 4, v15
	v_lshl_or_b32 v16, v2, 8, v15
	v_add_u32_e32 v20, 0xc800, v16
	v_add_u32_e32 v15, 4, v3
	v_xor_b32_e32 v15, v15, v2
	v_lshlrev_b32_e32 v15, 4, v15
	v_lshl_or_b32 v17, v2, 8, v15
	v_add_u32_e32 v21, 0xc800, v17
	v_add_u32_e32 v15, 8, v3
	v_xor_b32_e32 v15, v15, v2
	v_lshlrev_b32_e32 v15, 4, v15
	v_lshl_or_b32 v18, v2, 8, v15
	v_add_u32_e32 v22, 0xc800, v18
	v_add_u32_e32 v15, 12, v3
	v_xor_b32_e32 v15, v15, v2
	v_lshlrev_b32_e32 v15, 4, v15
	v_lshl_or_b32 v19, v2, 8, v15
	v_add_u32_e32 v23, 0xc800, v19
	v_lshrrev_b32_e32 v188, 1, v3
	v_and_b32_e32 v189, 7, v14
	v_and_b32_e32 v190, 1, v3
	v_lshlrev_b32_e32 v190, 3, v190
	v_lshl_or_b32 v190, v14, 7, v190
	v_add_u32_e32 v15, 0, v188
	v_xor_b32_e32 v15, v15, v189
	v_lshl_add_u32 v24, v15, 4, v190
	v_add_u32_e32 v28, 0xc800, v24
	v_add_u32_e32 v15, 2, v188
	v_xor_b32_e32 v15, v15, v189
	v_lshl_add_u32 v25, v15, 4, v190
	v_add_u32_e32 v29, 0xc800, v25
	v_add_u32_e32 v15, 4, v188
	v_xor_b32_e32 v15, v15, v189
	v_lshl_add_u32 v26, v15, 4, v190
	v_add_u32_e32 v30, 0xc800, v26
	v_add_u32_e32 v15, 6, v188
	v_xor_b32_e32 v15, v15, v189
	v_lshl_add_u32 v27, v15, 4, v190
	v_add_u32_e32 v31, 0xc800, v27
	v_lshlrev_b32_e32 v242, 12, v14
	v_lshl_add_u32 v242, v3, 3, v242
	v_lshlrev_b32_e32 v36, 2, v14
	v_add_u32_e32 v37, 0xc800, v36
	v_lshlrev_b32_e32 v38, 5, v3
	v_add_u32_e32 v39, 0xc800, v38
	s_and_b32 s45, s41, 1
	s_lshl_b32 s45, s45, 4
	v_add_u32_e32 v43, s45, v2
	v_lshlrev_b32_e32 v189, 3, v3
	v_sub_u32_e32 v43, v43, v189
	v_cmp_le_i32_e64 s[52:53], 0, v43
	v_cmp_le_i32_e64 s[54:55], 1, v43
	v_cmp_le_i32_e64 s[56:57], 2, v43
	v_cmp_le_i32_e64 s[58:59], 3, v43
	v_cmp_le_i32_e64 s[60:61], 4, v43
	v_cmp_le_i32_e64 s[62:63], 5, v43
	v_cmp_le_i32_e64 s[64:65], 6, v43
	v_cmp_le_i32_e64 s[66:67], 7, v43
	v_cmp_eq_u32_e32 vcc, 0, v43
	s_nop 1
	v_cndmask_b32_e64 v188, 0, 1.0, vcc
	v_cmp_eq_u32_e32 vcc, 1, v43
	s_nop 1
	v_cndmask_b32_e64 v189, 0, 1.0, vcc
	v_cmp_eq_u32_e32 vcc, 2, v43
	s_nop 1
	v_cndmask_b32_e64 v190, 0, 1.0, vcc
	v_cmp_eq_u32_e32 vcc, 3, v43
	s_nop 1
	v_cndmask_b32_e64 v191, 0, 1.0, vcc
	v_cmp_eq_u32_e32 vcc, 4, v43
	s_nop 1
	v_cndmask_b32_e64 v192, 0, 1.0, vcc
	v_cmp_eq_u32_e32 vcc, 5, v43
	s_nop 1
	v_cndmask_b32_e64 v193, 0, 1.0, vcc
	v_cmp_eq_u32_e32 vcc, 6, v43
	s_nop 1
	v_cndmask_b32_e64 v194, 0, 1.0, vcc
	v_cmp_eq_u32_e32 vcc, 7, v43
	s_nop 1
	v_cndmask_b32_e64 v195, 0, 1.0, vcc
	v_cvt_pk_f16_f32 v92, v188, v189
	v_cvt_pk_f16_f32 v93, v190, v191
	v_cvt_pk_f16_f32 v94, v192, v193
	v_cvt_pk_f16_f32 v95, v194, v195
	v_mov_b32_e32 v250, 0
	v_mov_b32_e32 v251, 0
	v_mov_b32_e32 v188, 0xffff
	v_mov_b32_e32 v189, 0xffff0000
	v_cndmask_b32_e64 v190, 0, v188, s[52:53]
	v_cndmask_b32_e64 v191, 0, v189, s[54:55]
	v_or_b32_e32 v244, v190, v191
	v_cndmask_b32_e64 v190, 0, v188, s[56:57]
	v_cndmask_b32_e64 v191, 0, v189, s[58:59]
	v_or_b32_e32 v245, v190, v191
	v_cndmask_b32_e64 v190, 0, v188, s[60:61]
	v_cndmask_b32_e64 v191, 0, v189, s[62:63]
	v_or_b32_e32 v246, v190, v191
	v_cndmask_b32_e64 v190, 0, v188, s[64:65]
	v_cndmask_b32_e64 v191, 0, v189, s[66:67]
	v_or_b32_e32 v247, v190, v191
	s_waitcnt lgkmcnt(0)
	s_lshl_b32 s45, s28, 12
	s_lshl_b32 s48, s27, 7
	s_add_u32 s45, s45, s48
	s_lshl_b32 s48, s45, 9
	s_add_u32 s48, s4, s48
	s_addc_u32 s49, s5, 0
	v_lshlrev_b32_e32 v188, 9, v14
	v_lshl_add_u32 v188, v3, 4, v188
	global_load_dwordx4 v[44:47], v188, s[48:49] offset:256
	global_load_dwordx4 v[48:51], v188, s[48:49] offset:320
	global_load_dwordx4 v[52:55], v188, s[48:49] offset:384
	global_load_dwordx4 v[56:59], v188, s[48:49] offset:448
	s_lshl_b32 s48, s28, 5
	s_add_u32 s48, s48, s27
	s_lshl_b32 s48, s48, 15
	s_add_u32 s48, s10, s48
	s_addc_u32 s49, s11, 0
	v_lshlrev_b32_e32 v188, 8, v14
	v_lshl_add_u32 v188, v3, 4, v188
	global_load_dwordx4 v[144:147], v188, s[48:49] offset:0
	global_load_dwordx4 v[148:151], v188, s[48:49] offset:64
	global_load_dwordx4 v[152:155], v188, s[48:49] offset:128
	global_load_dwordx4 v[156:159], v188, s[48:49] offset:192
	v_and_b32_e32 v188, 7, v42
	v_add_u32_e32 v188, s29, v188
	v_lshlrev_b32_e32 v188, 2, v188
	global_load_dword v11, v188, s[20:21]
	global_load_dword v12, v188, s[18:19]
	s_mul_i32 s48, s28, 0x900
	s_lshl_b32 s49, s29, 6
	s_add_u32 s48, s48, s49
	s_lshl_b32 s48, s48, 13
	s_lshl_b32 s49, s27, 8
	s_add_u32 s48, s48, s49
	s_add_u32 s30, s6, s48
	s_addc_u32 s31, s7, 0
	s_lshl_b32 s48, s28, 5
	s_add_u32 s48, s48, s27
	s_lshl_b32 s48, s48, 5
	s_add_u32 s48, s48, s29
	s_lshl_b32 s48, s48, 14
	s_add_u32 s32, s12, s48
	s_addc_u32 s33, s13, 0
	s_lshl_b32 s48, s45, 12
	s_lshl_b32 s49, s29, 7
	s_add_u32 s48, s48, s49
	s_add_u32 s34, s8, s48
	s_addc_u32 s35, s9, 0
	s_add_u32 s38, s22, s48
	s_addc_u32 s39, s23, 0
	s_lshl_b32 s48, s28, 5
	s_add_u32 s48, s48, s29
	s_lshl_b32 s48, s48, 14
	s_lshl_b32 s49, s27, 9
	s_add_u32 s48, s48, s49
	s_lshr_b32 s49, s40, 1
	s_cmp_eq_u32 s49, 1
	s_cselect_b32 s50, s14, s16
	s_cselect_b32 s51, s15, s17
	s_add_u32 s36, s50, s48
	s_addc_u32 s37, s51, 0
	s_lshl_b32 s48, s45, 2
	s_add_u32 s24, s24, s48
	s_addc_u32 s25, s25, 0
	v_lshlrev_b32_e32 v15, 2, v14
	s_mov_b32 s51, 0xbfb8aa3b
	s_mov_b32 s50, 0x41800000
	s_add_u32 m0, s43, 0x0
	s_nop 0
	global_load_lds_dwordx4 v4, s[30:31]
	s_add_u32 m0, s43, 0x4000
	s_nop 0
	global_load_lds_dwordx4 v6, s[32:33]
	s_add_u32 m0, s43, 0x8000
	s_nop 0
	global_load_lds_dwordx4 v8, s[34:35]
	s_add_u32 m0, s43, 0x2000
	s_nop 0
	global_load_lds_dwordx4 v5, s[30:31]
	s_add_u32 m0, s43, 0x6000
	s_nop 0
	global_load_lds_dwordx4 v7, s[32:33]
	s_add_u32 m0, s43, 0xa000
	s_nop 0
	global_load_lds_dwordx4 v9, s[34:35]
	s_add_u32 m0, s44, 0xc000
	s_nop 0
	global_load_lds_dword v10, s[36:37]
	s_add_u32 s30, s30, 0x80000
	s_addc_u32 s31, s31, 0
	s_add_u32 s32, s32, 0x4000
	s_addc_u32 s33, s33, 0
	s_add_u32 s34, s34, 0x80
	s_addc_u32 s35, s35, 0
	s_add_u32 s36, s36, 0x4000
	s_addc_u32 s37, s37, 0
	global_load_dword v243, v10, s[36:37]
	global_load_dword v243, v10, s[36:37]
	global_load_dword v243, v10, s[36:37]
	global_load_dword v243, v10, s[36:37]
	s_waitcnt vmcnt(16)
	v_cvt_f32_f16_e32 v60, v144
	v_cvt_f32_f16_sdwa v61, v144 dst_sel:DWORD dst_unused:UNUSED_PAD src0_sel:WORD_1
	v_cvt_f32_f16_e32 v62, v145
	v_cvt_f32_f16_sdwa v63, v145 dst_sel:DWORD dst_unused:UNUSED_PAD src0_sel:WORD_1
	v_cvt_f32_f16_e32 v64, v146
	v_cvt_f32_f16_sdwa v65, v146 dst_sel:DWORD dst_unused:UNUSED_PAD src0_sel:WORD_1
	v_cvt_f32_f16_e32 v66, v147
	v_cvt_f32_f16_sdwa v67, v147 dst_sel:DWORD dst_unused:UNUSED_PAD src0_sel:WORD_1
	s_waitcnt vmcnt(15)
	v_cvt_f32_f16_e32 v68, v148
	v_cvt_f32_f16_sdwa v69, v148 dst_sel:DWORD dst_unused:UNUSED_PAD src0_sel:WORD_1
	v_cvt_f32_f16_e32 v70, v149
	v_cvt_f32_f16_sdwa v71, v149 dst_sel:DWORD dst_unused:UNUSED_PAD src0_sel:WORD_1
	v_cvt_f32_f16_e32 v72, v150
	v_cvt_f32_f16_sdwa v73, v150 dst_sel:DWORD dst_unused:UNUSED_PAD src0_sel:WORD_1
	v_cvt_f32_f16_e32 v74, v151
	v_cvt_f32_f16_sdwa v75, v151 dst_sel:DWORD dst_unused:UNUSED_PAD src0_sel:WORD_1
	s_waitcnt vmcnt(14)
	v_cvt_f32_f16_e32 v76, v152
	v_cvt_f32_f16_sdwa v77, v152 dst_sel:DWORD dst_unused:UNUSED_PAD src0_sel:WORD_1
	v_cvt_f32_f16_e32 v78, v153
	v_cvt_f32_f16_sdwa v79, v153 dst_sel:DWORD dst_unused:UNUSED_PAD src0_sel:WORD_1
	v_cvt_f32_f16_e32 v80, v154
	v_cvt_f32_f16_sdwa v81, v154 dst_sel:DWORD dst_unused:UNUSED_PAD src0_sel:WORD_1
	v_cvt_f32_f16_e32 v82, v155
	v_cvt_f32_f16_sdwa v83, v155 dst_sel:DWORD dst_unused:UNUSED_PAD src0_sel:WORD_1
	s_waitcnt vmcnt(13)
	v_cvt_f32_f16_e32 v84, v156
	v_cvt_f32_f16_sdwa v85, v156 dst_sel:DWORD dst_unused:UNUSED_PAD src0_sel:WORD_1
	v_cvt_f32_f16_e32 v86, v157
	v_cvt_f32_f16_sdwa v87, v157 dst_sel:DWORD dst_unused:UNUSED_PAD src0_sel:WORD_1
	v_cvt_f32_f16_e32 v88, v158
	v_cvt_f32_f16_sdwa v89, v158 dst_sel:DWORD dst_unused:UNUSED_PAD src0_sel:WORD_1
	v_cvt_f32_f16_e32 v90, v159
	v_cvt_f32_f16_sdwa v91, v159 dst_sel:DWORD dst_unused:UNUSED_PAD src0_sel:WORD_1
	s_waitcnt vmcnt(11)
	s_waitcnt vmcnt(12)
	v_mul_f32_e32 v11, 0x41800000, v11
	s_mov_b32 s48, 0

.Lmy_s2_diag5:
	ds_read_b64 v[234:235], v24 offset:32768
	ds_read_b64 v[236:237], v25 offset:32768
	ds_read_b64 v[238:239], v26 offset:32768
	ds_read_b64 v[240:241], v27 offset:32768
	s_waitcnt lgkmcnt(4)
	v_fma_f32 v188, v188, s51, v189
	v_exp_f32_e32 v188, v188
	s_nop 0
	v_pk_mul_f32 v[176:177], v[176:177], v[188:189] op_sel_hi:[1,0]
	v_pk_mul_f32 v[178:179], v[178:179], v[188:189] op_sel_hi:[1,0]
	v_pk_mul_f32 v[180:181], v[180:181], v[188:189] op_sel_hi:[1,0]
	v_pk_mul_f32 v[182:183], v[182:183], v[188:189] op_sel_hi:[1,0]
	v_pk_mul_f32 v[176:177], v[60:61], v[176:177]
	v_pk_mul_f32 v[178:179], v[62:63], v[178:179]
	v_pk_mul_f32 v[180:181], v[64:65], v[180:181]
	v_pk_mul_f32 v[182:183], v[66:67], v[182:183]
	v_cvt_pk_f16_f32 v184, v176, v177
	v_cvt_pk_f16_f32 v185, v178, v179
	v_cvt_pk_f16_f32 v186, v180, v181
	v_cvt_pk_f16_f32 v187, v182, v183
	v_and_b32_e32 v184, v244, v184
	v_and_b32_e32 v185, v245, v185
	v_and_b32_e32 v186, v246, v186
	v_and_b32_e32 v187, v247, v187
	s_nop 1
	v_mfma_f32_16x16x32_f16 v[112:115], v[144:147], v[184:187], 0
	v_mfma_f32_16x16x32_f16 v[116:119], v[148:151], v[184:187], 0
	v_mfma_f32_16x16x32_f16 v[120:123], v[152:155], v[184:187], 0
	v_mfma_f32_16x16x32_f16 v[124:127], v[156:159], v[184:187], 0
	v_mfma_f32_16x16x32_f16 v[128:131], v[144:147], v[92:95], 0
	v_mfma_f32_16x16x32_f16 v[132:135], v[148:151], v[92:95], 0
	v_mfma_f32_16x16x32_f16 v[136:139], v[152:155], v[92:95], 0
	v_mfma_f32_16x16x32_f16 v[140:143], v[156:159], v[92:95], 0
	s_branch .Lmy_s2_kend4

.Lmy_s2_diag7:
	ds_read_b64 v[234:235], v24 offset:32768
	ds_read_b64 v[236:237], v25 offset:32768
	ds_read_b64 v[238:239], v26 offset:32768
	ds_read_b64 v[240:241], v27 offset:32768
	s_waitcnt lgkmcnt(4)
	v_fma_f32 v232, v232, s51, v189
	v_exp_f32_e32 v232, v232
	s_nop 0
	v_pk_mul_f32 v[224:225], v[224:225], v[232:233] op_sel_hi:[1,0]
	v_pk_mul_f32 v[226:227], v[226:227], v[232:233] op_sel_hi:[1,0]
	v_pk_mul_f32 v[228:229], v[228:229], v[232:233] op_sel_hi:[1,0]
	v_pk_mul_f32 v[230:231], v[230:231], v[232:233] op_sel_hi:[1,0]
	v_pk_mul_f32 v[224:225], v[68:69], v[224:225]
	v_pk_mul_f32 v[226:227], v[70:71], v[226:227]
	v_pk_mul_f32 v[228:229], v[72:73], v[228:229]
	v_pk_mul_f32 v[230:231], v[74:75], v[230:231]
	v_cvt_pk_f16_f32 v184, v224, v225
	v_cvt_pk_f16_f32 v185, v226, v227
	v_cvt_pk_f16_f32 v186, v228, v229
	v_cvt_pk_f16_f32 v187, v230, v231
	v_and_b32_e32 v184, v244, v184
	v_and_b32_e32 v185, v245, v185
	v_and_b32_e32 v186, v246, v186
	v_and_b32_e32 v187, v247, v187
	s_nop 1
	v_mfma_f32_16x16x32_f16 v[112:115], v[160:163], v[184:187], v[112:115]
	v_mfma_f32_16x16x32_f16 v[116:119], v[164:167], v[184:187], v[116:119]
	v_mfma_f32_16x16x32_f16 v[120:123], v[168:171], v[184:187], v[120:123]
	v_mfma_f32_16x16x32_f16 v[124:127], v[172:175], v[184:187], v[124:127]
	v_mfma_f32_16x16x32_f16 v[128:131], v[160:163], v[92:95], 0
	v_mfma_f32_16x16x32_f16 v[132:135], v[164:167], v[92:95], 0
	v_mfma_f32_16x16x32_f16 v[136:139], v[168:171], v[92:95], 0
	v_mfma_f32_16x16x32_f16 v[140:143], v[172:175], v[92:95], 0
	s_branch .Lmy_s2_kend4

.Lmy_s2_diag9:
	ds_read_b64 v[234:235], v24 offset:32768
	ds_read_b64 v[236:237], v25 offset:32768
	ds_read_b64 v[238:239], v26 offset:32768
	ds_read_b64 v[240:241], v27 offset:32768
	s_waitcnt lgkmcnt(4)
	v_fma_f32 v188, v188, s51, v189
	v_exp_f32_e32 v188, v188
	s_nop 0
	v_pk_mul_f32 v[176:177], v[176:177], v[188:189] op_sel_hi:[1,0]
	v_pk_mul_f32 v[178:179], v[178:179], v[188:189] op_sel_hi:[1,0]
	v_pk_mul_f32 v[180:181], v[180:181], v[188:189] op_sel_hi:[1,0]
	v_pk_mul_f32 v[182:183], v[182:183], v[188:189] op_sel_hi:[1,0]
	v_pk_mul_f32 v[176:177], v[76:77], v[176:177]
	v_pk_mul_f32 v[178:179], v[78:79], v[178:179]
	v_pk_mul_f32 v[180:181], v[80:81], v[180:181]
	v_pk_mul_f32 v[182:183], v[82:83], v[182:183]
	v_cvt_pk_f16_f32 v184, v176, v177
	v_cvt_pk_f16_f32 v185, v178, v179
	v_cvt_pk_f16_f32 v186, v180, v181
	v_cvt_pk_f16_f32 v187, v182, v183
	v_and_b32_e32 v184, v244, v184
	v_and_b32_e32 v185, v245, v185
	v_and_b32_e32 v186, v246, v186
	v_and_b32_e32 v187, v247, v187
	s_nop 1
	v_mfma_f32_16x16x32_f16 v[112:115], v[144:147], v[184:187], v[112:115]
	v_mfma_f32_16x16x32_f16 v[116:119], v[148:151], v[184:187], v[116:119]
	v_mfma_f32_16x16x32_f16 v[120:123], v[152:155], v[184:187], v[120:123]
	v_mfma_f32_16x16x32_f16 v[124:127], v[156:159], v[184:187], v[124:127]
	v_mfma_f32_16x16x32_f16 v[128:131], v[144:147], v[92:95], 0
	v_mfma_f32_16x16x32_f16 v[132:135], v[148:151], v[92:95], 0
	v_mfma_f32_16x16x32_f16 v[136:139], v[152:155], v[92:95], 0
	v_mfma_f32_16x16x32_f16 v[140:143], v[156:159], v[92:95], 0
	s_branch .Lmy_s2_kend4

.Lmy_s2_diag11:
	ds_read_b64 v[234:235], v24 offset:32768
	ds_read_b64 v[236:237], v25 offset:32768
	ds_read_b64 v[238:239], v26 offset:32768
	ds_read_b64 v[240:241], v27 offset:32768
	s_waitcnt lgkmcnt(4)
	v_fma_f32 v232, v232, s51, v189
	v_exp_f32_e32 v232, v232
	s_nop 0
	v_pk_mul_f32 v[224:225], v[224:225], v[232:233] op_sel_hi:[1,0]
	v_pk_mul_f32 v[226:227], v[226:227], v[232:233] op_sel_hi:[1,0]
	v_pk_mul_f32 v[228:229], v[228:229], v[232:233] op_sel_hi:[1,0]
	v_pk_mul_f32 v[230:231], v[230:231], v[232:233] op_sel_hi:[1,0]
	v_pk_mul_f32 v[224:225], v[84:85], v[224:225]
	v_pk_mul_f32 v[226:227], v[86:87], v[226:227]
	v_pk_mul_f32 v[228:229], v[88:89], v[228:229]
	v_pk_mul_f32 v[230:231], v[90:91], v[230:231]
	v_cvt_pk_f16_f32 v184, v224, v225
	v_cvt_pk_f16_f32 v185, v226, v227
	v_cvt_pk_f16_f32 v186, v228, v229
	v_cvt_pk_f16_f32 v187, v230, v231
	v_and_b32_e32 v184, v244, v184
	v_and_b32_e32 v185, v245, v185
	v_and_b32_e32 v186, v246, v186
	v_and_b32_e32 v187, v247, v187
	s_nop 1
	v_mfma_f32_16x16x32_f16 v[112:115], v[160:163], v[184:187], v[112:115]
	v_mfma_f32_16x16x32_f16 v[116:119], v[164:167], v[184:187], v[116:119]
	v_mfma_f32_16x16x32_f16 v[120:123], v[168:171], v[184:187], v[120:123]
	v_mfma_f32_16x16x32_f16 v[124:127], v[172:175], v[184:187], v[124:127]
	v_mfma_f32_16x16x32_f16 v[128:131], v[160:163], v[92:95], 0
	v_mfma_f32_16x16x32_f16 v[132:135], v[164:167], v[92:95], 0
	v_mfma_f32_16x16x32_f16 v[136:139], v[168:171], v[92:95], 0
	v_mfma_f32_16x16x32_f16 v[140:143], v[172:175], v[92:95], 0
	s_branch .Lmy_s2_kend4

.Lmy_s2_diag15:
	ds_read_b64 v[234:235], v28 offset:32768
	ds_read_b64 v[236:237], v29 offset:32768
	ds_read_b64 v[238:239], v30 offset:32768
	ds_read_b64 v[240:241], v31 offset:32768
	s_waitcnt lgkmcnt(4)
	v_fma_f32 v188, v188, s51, v189
	v_exp_f32_e32 v188, v188
	s_nop 0
	v_pk_mul_f32 v[176:177], v[176:177], v[188:189] op_sel_hi:[1,0]
	v_pk_mul_f32 v[178:179], v[178:179], v[188:189] op_sel_hi:[1,0]
	v_pk_mul_f32 v[180:181], v[180:181], v[188:189] op_sel_hi:[1,0]
	v_pk_mul_f32 v[182:183], v[182:183], v[188:189] op_sel_hi:[1,0]
	v_pk_mul_f32 v[176:177], v[60:61], v[176:177]
	v_pk_mul_f32 v[178:179], v[62:63], v[178:179]
	v_pk_mul_f32 v[180:181], v[64:65], v[180:181]
	v_pk_mul_f32 v[182:183], v[66:67], v[182:183]
	v_cvt_pk_f16_f32 v184, v176, v177
	v_cvt_pk_f16_f32 v185, v178, v179
	v_cvt_pk_f16_f32 v186, v180, v181
	v_cvt_pk_f16_f32 v187, v182, v183
	v_and_b32_e32 v184, v244, v184
	v_and_b32_e32 v185, v245, v185
	v_and_b32_e32 v186, v246, v186
	v_and_b32_e32 v187, v247, v187
	s_nop 1
	v_mfma_f32_16x16x32_f16 v[112:115], v[144:147], v[184:187], 0
	v_mfma_f32_16x16x32_f16 v[116:119], v[148:151], v[184:187], 0
	v_mfma_f32_16x16x32_f16 v[120:123], v[152:155], v[184:187], 0
	v_mfma_f32_16x16x32_f16 v[124:127], v[156:159], v[184:187], 0
	v_mfma_f32_16x16x32_f16 v[128:131], v[144:147], v[92:95], 0
	v_mfma_f32_16x16x32_f16 v[132:135], v[148:151], v[92:95], 0
	v_mfma_f32_16x16x32_f16 v[136:139], v[152:155], v[92:95], 0
	v_mfma_f32_16x16x32_f16 v[140:143], v[156:159], v[92:95], 0
	s_branch .Lmy_s2_kend14

.Lmy_s2_diag17:
	ds_read_b64 v[234:235], v28 offset:32768
	ds_read_b64 v[236:237], v29 offset:32768
	ds_read_b64 v[238:239], v30 offset:32768
	ds_read_b64 v[240:241], v31 offset:32768
	s_waitcnt lgkmcnt(4)
	v_fma_f32 v232, v232, s51, v189
	v_exp_f32_e32 v232, v232
	s_nop 0
	v_pk_mul_f32 v[224:225], v[224:225], v[232:233] op_sel_hi:[1,0]
	v_pk_mul_f32 v[226:227], v[226:227], v[232:233] op_sel_hi:[1,0]
	v_pk_mul_f32 v[228:229], v[228:229], v[232:233] op_sel_hi:[1,0]
	v_pk_mul_f32 v[230:231], v[230:231], v[232:233] op_sel_hi:[1,0]
	v_pk_mul_f32 v[224:225], v[68:69], v[224:225]
	v_pk_mul_f32 v[226:227], v[70:71], v[226:227]
	v_pk_mul_f32 v[228:229], v[72:73], v[228:229]
	v_pk_mul_f32 v[230:231], v[74:75], v[230:231]
	v_cvt_pk_f16_f32 v184, v224, v225
	v_cvt_pk_f16_f32 v185, v226, v227
	v_cvt_pk_f16_f32 v186, v228, v229
	v_cvt_pk_f16_f32 v187, v230, v231
	v_and_b32_e32 v184, v244, v184
	v_and_b32_e32 v185, v245, v185
	v_and_b32_e32 v186, v246, v186
	v_and_b32_e32 v187, v247, v187
	s_nop 1
	v_mfma_f32_16x16x32_f16 v[112:115], v[160:163], v[184:187], v[112:115]
	v_mfma_f32_16x16x32_f16 v[116:119], v[164:167], v[184:187], v[116:119]
	v_mfma_f32_16x16x32_f16 v[120:123], v[168:171], v[184:187], v[120:123]
	v_mfma_f32_16x16x32_f16 v[124:127], v[172:175], v[184:187], v[124:127]
	v_mfma_f32_16x16x32_f16 v[128:131], v[160:163], v[92:95], 0
	v_mfma_f32_16x16x32_f16 v[132:135], v[164:167], v[92:95], 0
	v_mfma_f32_16x16x32_f16 v[136:139], v[168:171], v[92:95], 0
	v_mfma_f32_16x16x32_f16 v[140:143], v[172:175], v[92:95], 0
	s_branch .Lmy_s2_kend14

.Lmy_s2_diag19:
	ds_read_b64 v[234:235], v28 offset:32768
	ds_read_b64 v[236:237], v29 offset:32768
	ds_read_b64 v[238:239], v30 offset:32768
	ds_read_b64 v[240:241], v31 offset:32768
	s_waitcnt lgkmcnt(4)
	v_fma_f32 v188, v188, s51, v189
	v_exp_f32_e32 v188, v188
	s_nop 0
	v_pk_mul_f32 v[176:177], v[176:177], v[188:189] op_sel_hi:[1,0]
	v_pk_mul_f32 v[178:179], v[178:179], v[188:189] op_sel_hi:[1,0]
	v_pk_mul_f32 v[180:181], v[180:181], v[188:189] op_sel_hi:[1,0]
	v_pk_mul_f32 v[182:183], v[182:183], v[188:189] op_sel_hi:[1,0]
	v_pk_mul_f32 v[176:177], v[76:77], v[176:177]
	v_pk_mul_f32 v[178:179], v[78:79], v[178:179]
	v_pk_mul_f32 v[180:181], v[80:81], v[180:181]
	v_pk_mul_f32 v[182:183], v[82:83], v[182:183]
	v_cvt_pk_f16_f32 v184, v176, v177
	v_cvt_pk_f16_f32 v185, v178, v179
	v_cvt_pk_f16_f32 v186, v180, v181
	v_cvt_pk_f16_f32 v187, v182, v183
	v_and_b32_e32 v184, v244, v184
	v_and_b32_e32 v185, v245, v185
	v_and_b32_e32 v186, v246, v186
	v_and_b32_e32 v187, v247, v187
	s_nop 1
	v_mfma_f32_16x16x32_f16 v[112:115], v[144:147], v[184:187], v[112:115]
	v_mfma_f32_16x16x32_f16 v[116:119], v[148:151], v[184:187], v[116:119]
	v_mfma_f32_16x16x32_f16 v[120:123], v[152:155], v[184:187], v[120:123]
	v_mfma_f32_16x16x32_f16 v[124:127], v[156:159], v[184:187], v[124:127]
	v_mfma_f32_16x16x32_f16 v[128:131], v[144:147], v[92:95], 0
	v_mfma_f32_16x16x32_f16 v[132:135], v[148:151], v[92:95], 0
	v_mfma_f32_16x16x32_f16 v[136:139], v[152:155], v[92:95], 0
	v_mfma_f32_16x16x32_f16 v[140:143], v[156:159], v[92:95], 0
	s_branch .Lmy_s2_kend14

.Lmy_s2_diag21:
	ds_read_b64 v[234:235], v28 offset:32768
	ds_read_b64 v[236:237], v29 offset:32768
	ds_read_b64 v[238:239], v30 offset:32768
	ds_read_b64 v[240:241], v31 offset:32768
	s_waitcnt lgkmcnt(4)
	v_fma_f32 v232, v232, s51, v189
	v_exp_f32_e32 v232, v232
	s_nop 0
	v_pk_mul_f32 v[224:225], v[224:225], v[232:233] op_sel_hi:[1,0]
	v_pk_mul_f32 v[226:227], v[226:227], v[232:233] op_sel_hi:[1,0]
	v_pk_mul_f32 v[228:229], v[228:229], v[232:233] op_sel_hi:[1,0]
	v_pk_mul_f32 v[230:231], v[230:231], v[232:233] op_sel_hi:[1,0]
	v_pk_mul_f32 v[224:225], v[84:85], v[224:225]
	v_pk_mul_f32 v[226:227], v[86:87], v[226:227]
	v_pk_mul_f32 v[228:229], v[88:89], v[228:229]
	v_pk_mul_f32 v[230:231], v[90:91], v[230:231]
	v_cvt_pk_f16_f32 v184, v224, v225
	v_cvt_pk_f16_f32 v185, v226, v227
	v_cvt_pk_f16_f32 v186, v228, v229
	v_cvt_pk_f16_f32 v187, v230, v231
	v_and_b32_e32 v184, v244, v184
	v_and_b32_e32 v185, v245, v185
	v_and_b32_e32 v186, v246, v186
	v_and_b32_e32 v187, v247, v187
	s_nop 1
	v_mfma_f32_16x16x32_f16 v[112:115], v[160:163], v[184:187], v[112:115]
	v_mfma_f32_16x16x32_f16 v[116:119], v[164:167], v[184:187], v[116:119]
	v_mfma_f32_16x16x32_f16 v[120:123], v[168:171], v[184:187], v[120:123]
	v_mfma_f32_16x16x32_f16 v[124:127], v[172:175], v[184:187], v[124:127]
	v_mfma_f32_16x16x32_f16 v[128:131], v[160:163], v[92:95], 0
	v_mfma_f32_16x16x32_f16 v[132:135], v[164:167], v[92:95], 0
	v_mfma_f32_16x16x32_f16 v[136:139], v[168:171], v[92:95], 0
	v_mfma_f32_16x16x32_f16 v[140:143], v[172:175], v[92:95], 0
	s_branch .Lmy_s2_kend14

	.amdhsa_kernel _Z12scan2_kernelPKDF16_S0_S0_S0_S0_PKfS2_S2_S2_PDF16_PfS4_
		.amdhsa_group_segment_fixed_size 34816
		.amdhsa_private_segment_fixed_size 0
		.amdhsa_kernarg_size 96
		.amdhsa_user_sgpr_count 2
		.amdhsa_user_sgpr_dispatch_ptr 0
		.amdhsa_user_sgpr_queue_ptr 0
		.amdhsa_user_sgpr_kernarg_segment_ptr 1
		.amdhsa_user_sgpr_dispatch_id 0
		.amdhsa_user_sgpr_kernarg_preload_length 0
		.amdhsa_user_sgpr_kernarg_preload_offset 0
		.amdhsa_user_sgpr_private_segment_size 0
		.amdhsa_uses_dynamic_stack 0
		.amdhsa_enable_private_segment 0
		.amdhsa_system_sgpr_workgroup_id_x 1
		.amdhsa_system_sgpr_workgroup_id_y 0
		.amdhsa_system_sgpr_workgroup_id_z 0
		.amdhsa_system_sgpr_workgroup_info 0
		.amdhsa_system_vgpr_workitem_id 0
		.amdhsa_next_free_vgpr 252
		.amdhsa_next_free_sgpr 80
		.amdhsa_accum_offset 252
		.amdhsa_reserve_vcc 1
		.amdhsa_float_round_mode_32 0
		.amdhsa_float_round_mode_16_64 0
		.amdhsa_float_denorm_mode_32 3
		.amdhsa_float_denorm_mode_16_64 3
		.amdhsa_dx10_clamp 1
		.amdhsa_ieee_mode 1
		.amdhsa_fp16_overflow 0
		.amdhsa_tg_split 0
		.amdhsa_exception_fp_ieee_invalid_op 0
		.amdhsa_exception_fp_denorm_src 0
		.amdhsa_exception_fp_ieee_div_zero 0
		.amdhsa_exception_fp_ieee_overflow 0
		.amdhsa_exception_fp_ieee_underflow 0
		.amdhsa_exception_fp_ieee_inexact 0
		.amdhsa_exception_int_div_zero 0
	.end_amdhsa_kernel

amdhsa.kernels:
  - .agpr_count:     0
    .args:
      - .actual_access:  read_only
        .address_space:  global
        .offset:         0
        .size:           8
        .value_kind:     global_buffer
      - .actual_access:  read_only
        .address_space:  global
        .offset:         8
        .size:           8
        .value_kind:     global_buffer
      - .actual_access:  read_only
        .address_space:  global
        .offset:         16
        .size:           8
        .value_kind:     global_buffer
      - .actual_access:  read_only
        .address_space:  global
        .offset:         24
        .size:           8
        .value_kind:     global_buffer
      - .actual_access:  write_only
        .address_space:  global
        .offset:         32
        .size:           8
        .value_kind:     global_buffer
      - .actual_access:  write_only
        .address_space:  global
        .offset:         40
        .size:           8
        .value_kind:     global_buffer
      - .actual_access:  write_only
        .address_space:  global
        .offset:         48
        .size:           8
        .value_kind:     global_buffer
      - .actual_access:  write_only
        .address_space:  global
        .offset:         56
        .size:           8
        .value_kind:     global_buffer
    .group_segment_fixed_size: 16640
    .kernarg_segment_align: 8
    .kernarg_segment_size: 64
    .language:       OpenCL C
    .language_version:
      - 2
      - 0
    .max_flat_workgroup_size: 256
    .name:           _Z11prep_kernelPKfS0_S0_S0_PDF16_S1_S1_Pf
    .private_segment_fixed_size: 0
    .sgpr_count:     18
    .sgpr_spill_count: 0
    .symbol:         _Z11prep_kernelPKfS0_S0_S0_PDF16_S1_S1_Pf.kd
    .uniform_work_group_size: 1
    .uses_dynamic_stack: false
    .vgpr_count:     42
    .vgpr_spill_count: 0
    .wavefront_size: 64
  - .agpr_count:     0
    .args:
      - .address_space:  global
        .offset:         0
        .size:           8
        .value_kind:     global_buffer
      - .address_space:  global
        .offset:         8
        .size:           8
        .value_kind:     global_buffer
      - .actual_access:  write_only
        .address_space:  global
        .offset:         16
        .size:           8
        .value_kind:     global_buffer
      - .actual_access:  read_only
        .address_space:  global
        .offset:         24
        .size:           8
        .value_kind:     global_buffer
    .group_segment_fixed_size: 49152
    .kernarg_segment_align: 8
    .kernarg_segment_size: 32
    .language:       OpenCL C
    .language_version:
      - 2
      - 0
    .max_flat_workgroup_size: 512
    .name:           _Z13gemm2b_kernelPKDF16_S0_PfPKf
    .private_segment_fixed_size: 0
    .sgpr_count:     24
    .sgpr_spill_count: 0
    .symbol:         _Z13gemm2b_kernelPKDF16_S0_PfPKf.kd
    .uniform_work_group_size: 1
    .uses_dynamic_stack: false
    .vgpr_count:     176
    .vgpr_spill_count: 0
    .wavefront_size: 64
  - .agpr_count:     0
    .args:
      - .address_space:  global
        .offset:         0
        .size:           8
        .value_kind:     global_buffer
      - .address_space:  global
        .offset:         8
        .size:           8
        .value_kind:     global_buffer
      - .actual_access:  write_only
        .address_space:  global
        .offset:         16
        .size:           8
        .value_kind:     global_buffer
      - .actual_access:  write_only
        .address_space:  global
        .offset:         24
        .size:           8
        .value_kind:     global_buffer
    .group_segment_fixed_size: 16384
    .kernarg_segment_align: 8
    .kernarg_segment_size: 32
    .language:       OpenCL C
    .language_version:
      - 2
      - 0
    .max_flat_workgroup_size: 512
    .name:           _Z12gemm8_kernelPKDF16_S0_PDF16_S1_
    .private_segment_fixed_size: 0
    .sgpr_count:     58
    .sgpr_spill_count: 0
    .symbol:         _Z12gemm8_kernelPKDF16_S0_PDF16_S1_.kd
    .uniform_work_group_size: 1
    .uses_dynamic_stack: false
    .vgpr_count:     184
    .vgpr_spill_count: 0
    .wavefront_size: 64
  - .agpr_count:     0
    .args:
      - .actual_access:  read_only
        .address_space:  global
        .offset:         0
        .size:           8
        .value_kind:     global_buffer
      - .actual_access:  read_only
        .address_space:  global
        .offset:         8
        .size:           8
        .value_kind:     global_buffer
      - .actual_access:  read_only
        .address_space:  global
        .offset:         16
        .size:           8
        .value_kind:     global_buffer
      - .actual_access:  read_only
        .address_space:  global
        .offset:         24
        .size:           8
        .value_kind:     global_buffer
      - .actual_access:  write_only
        .address_space:  global
        .offset:         32
        .size:           8
        .value_kind:     global_buffer
      - .actual_access:  write_only
        .address_space:  global
        .offset:         40
        .size:           8
        .value_kind:     global_buffer
      - .actual_access:  read_only
        .address_space:  global
        .offset:         48
        .size:           8
        .value_kind:     global_buffer
      - .actual_access:  read_only
        .address_space:  global
        .offset:         56
        .size:           8
        .value_kind:     global_buffer
      - .actual_access:  read_only
        .address_space:  global
        .offset:         64
        .size:           8
        .value_kind:     global_buffer
      - .actual_access:  write_only
        .address_space:  global
        .offset:         72
        .size:           8
        .value_kind:     global_buffer
      - .actual_access:  write_only
        .address_space:  global
        .offset:         80
        .size:           8
        .value_kind:     global_buffer
      - .actual_access:  write_only
        .address_space:  global
        .offset:         88
        .size:           8
        .value_kind:     global_buffer
      - .actual_access:  write_only
        .address_space:  global
        .offset:         96
        .size:           8
        .value_kind:     global_buffer
    .group_segment_fixed_size: 17952
    .kernarg_segment_align: 8
    .kernarg_segment_size: 104
    .language:       OpenCL C
    .language_version:
      - 2
      - 0
    .max_flat_workgroup_size: 256
    .name:           _Z13convdt_kernelPKDF16_S0_PKfS2_PDF16_S3_S2_S2_S2_PfS4_S4_S4_
    .private_segment_fixed_size: 0
    .sgpr_count:     26
    .sgpr_spill_count: 0
    .symbol:         _Z13convdt_kernelPKDF16_S0_PKfS2_PDF16_S3_S2_S2_S2_PfS4_S4_S4_.kd
    .uniform_work_group_size: 1
    .uses_dynamic_stack: false
    .vgpr_count:     88
    .vgpr_spill_count: 0
    .wavefront_size: 64
  - .agpr_count:     0
    .args:
      - .actual_access:  read_only
        .address_space:  global
        .offset:         0
        .size:           8
        .value_kind:     global_buffer
      - .actual_access:  read_only
        .address_space:  global
        .offset:         8
        .size:           8
        .value_kind:     global_buffer
      - .actual_access:  read_only
        .address_space:  global
        .offset:         16
        .size:           8
        .value_kind:     global_buffer
      - .actual_access:  write_only
        .address_space:  global
        .offset:         24
        .size:           8
        .value_kind:     global_buffer
    .group_segment_fixed_size: 34816
    .kernarg_segment_align: 8
    .kernarg_segment_size: 32
    .language:       OpenCL C
    .language_version:
      - 2
      - 0
    .max_flat_workgroup_size: 256
    .name:           _Z11sloc_kernelPKDF16_PKfS2_PDF16_
    .private_segment_fixed_size: 0
    .sgpr_count:     28
    .sgpr_spill_count: 0
    .symbol:         _Z11sloc_kernelPKDF16_PKfS2_PDF16_.kd
    .uniform_work_group_size: 1
    .uses_dynamic_stack: false
    .vgpr_count:     120
    .vgpr_spill_count: 0
    .wavefront_size: 64
  - .agpr_count:     64
    .args:
      - .actual_access:  read_only
        .address_space:  global
        .offset:         0
        .size:           8
        .value_kind:     global_buffer
      - .address_space:  global
        .offset:         8
        .size:           8
        .value_kind:     global_buffer
      - .actual_access:  read_only
        .address_space:  global
        .offset:         16
        .size:           8
        .value_kind:     global_buffer
      - .actual_access:  write_only
        .address_space:  global
        .offset:         24
        .size:           8
        .value_kind:     global_buffer
    .group_segment_fixed_size: 0
    .kernarg_segment_align: 8
    .kernarg_segment_size: 32
    .language:       OpenCL C
    .language_version:
      - 2
      - 0
    .max_flat_workgroup_size: 256
    .name:           _Z12spass_kernelPKfPDF16_PKDF16_S1_
    .private_segment_fixed_size: 0
    .sgpr_count:     21
    .sgpr_spill_count: 0
    .symbol:         _Z12spass_kernelPKfPDF16_PKDF16_S1_.kd
    .uniform_work_group_size: 1
    .uses_dynamic_stack: false
    .vgpr_count:     180
    .vgpr_spill_count: 0
    .wavefront_size: 64
  - .agpr_count:     0
    .args:
      - .actual_access:  read_only
        .address_space:  global
        .offset:         0
        .size:           8
        .value_kind:     global_buffer
      - .actual_access:  read_only
        .address_space:  global
        .offset:         8
        .size:           8
        .value_kind:     global_buffer
      - .actual_access:  read_only
        .address_space:  global
        .offset:         16
        .size:           8
        .value_kind:     global_buffer
      - .actual_access:  read_only
        .address_space:  global
        .offset:         24
        .size:           8
        .value_kind:     global_buffer
      - .actual_access:  read_only
        .address_space:  global
        .offset:         32
        .size:           8
        .value_kind:     global_buffer
      - .actual_access:  read_only
        .address_space:  global
        .offset:         40
        .size:           8
        .value_kind:     global_buffer
      - .actual_access:  read_only
        .address_space:  global
        .offset:         48
        .size:           8
        .value_kind:     global_buffer
      - .actual_access:  read_only
        .address_space:  global
        .offset:         56
        .size:           8
        .value_kind:     global_buffer
      - .actual_access:  read_only
        .address_space:  global
        .offset:         64
        .size:           8
        .value_kind:     global_buffer
      - .actual_access:  write_only
        .address_space:  global
        .offset:         72
        .size:           8
        .value_kind:     global_buffer
      - .address_space:  global
        .offset:         80
        .size:           8
        .value_kind:     global_buffer
      - .actual_access:  read_only
        .address_space:  global
        .offset:         88
        .size:           8
        .value_kind:     global_buffer
    .group_segment_fixed_size: 54272
    .kernarg_segment_align: 8
    .kernarg_segment_size: 96
    .language:       OpenCL C
    .language_version:
      - 2
      - 0
    .max_flat_workgroup_size: 256
    .name:           _Z11scan_kernelPKDF16_S0_S0_S0_S0_PKfS2_S2_S2_PDF16_PfS4_
    .private_segment_fixed_size: 0
    .sgpr_count:     106
    .sgpr_spill_count: 56
    .symbol:         _Z11scan_kernelPKDF16_S0_S0_S0_S0_PKfS2_S2_S2_PDF16_PfS4_.kd
    .uniform_work_group_size: 1
    .uses_dynamic_stack: false
    .vgpr_count:     243
    .vgpr_spill_count: 0
    .wavefront_size: 64
  - .agpr_count:     0
    .args:
      - .actual_access:  read_only
        .address_space:  global
        .offset:         0
        .size:           8
        .value_kind:     global_buffer
      - .address_space:  global
        .offset:         8
        .size:           8
        .value_kind:     global_buffer
      - .address_space:  global
        .offset:         16
        .size:           8
        .value_kind:     global_buffer
      - .actual_access:  read_only
        .address_space:  global
        .offset:         24
        .size:           8
        .value_kind:     global_buffer
      - .address_space:  global
        .offset:         32
        .size:           8
        .value_kind:     global_buffer
      - .address_space:  global
        .offset:         40
        .size:           8
        .value_kind:     global_buffer
      - .address_space:  global
        .offset:         48
        .size:           8
        .value_kind:     global_buffer
      - .actual_access:  read_only
        .address_space:  global
        .offset:         56
        .size:           8
        .value_kind:     global_buffer
      - .actual_access:  read_only
        .address_space:  global
        .offset:         64
        .size:           8
        .value_kind:     global_buffer
      - .actual_access:  write_only
        .address_space:  global
        .offset:         72
        .size:           8
        .value_kind:     global_buffer
      - .address_space:  global
        .offset:         80
        .size:           8
        .value_kind:     global_buffer
      - .actual_access:  read_only
        .address_space:  global
        .offset:         88
        .size:           8
        .value_kind:     global_buffer
    .group_segment_fixed_size: 34816
    .kernarg_segment_align: 8
    .kernarg_segment_size: 96
    .language:       OpenCL C
    .language_version:
      - 2
      - 0
    .max_flat_workgroup_size: 512
    .name:           _Z12scan2_kernelPKDF16_S0_S0_S0_S0_PKfS2_S2_S2_PDF16_PfS4_
    .private_segment_fixed_size: 0
    .sgpr_count:     86
    .sgpr_spill_count: 0
    .symbol:         _Z12scan2_kernelPKDF16_S0_S0_S0_S0_PKfS2_S2_S2_PDF16_PfS4_.kd
    .uniform_work_group_size: 1
    .uses_dynamic_stack: false
    .vgpr_count:     252
    .vgpr_spill_count: 0
    .wavefront_size: 64
  - .agpr_count:     64
    .args:
      - .address_space:  global
        .offset:         0
        .size:           8
        .value_kind:     global_buffer
      - .address_space:  global
        .offset:         8
        .size:           8
        .value_kind:     global_buffer
      - .offset:         16
        .size:           4
        .value_kind:     by_value
      - .offset:         20
        .size:           4
        .value_kind:     by_value
      - .offset:         24
        .size:           4
        .value_kind:     by_value
      - .actual_access:  write_only
        .address_space:  global
        .offset:         32
        .size:           8
        .value_kind:     global_buffer
      - .actual_access:  write_only
        .address_space:  global
        .offset:         40
        .size:           8
        .value_kind:     global_buffer
      - .actual_access:  read_only
        .address_space:  global
        .offset:         48
        .size:           8
        .value_kind:     global_buffer
      - .offset:         56
        .size:           4
        .value_kind:     by_value
    .group_segment_fixed_size: 131072
    .kernarg_segment_align: 8
    .kernarg_segment_size: 60
    .language:       OpenCL C
    .language_version:
      - 2
      - 0
    .max_flat_workgroup_size: 256
    .name:           _Z11gemm_kernelILi1EEvPKDF16_S1_iiiPDF16_PfPKfi
    .private_segment_fixed_size: 0
    .sgpr_count:     27
    .sgpr_spill_count: 0
    .symbol:         _Z11gemm_kernelILi1EEvPKDF16_S1_iiiPDF16_PfPKfi.kd
    .uniform_work_group_size: 1
    .uses_dynamic_stack: false
    .vgpr_count:     208
    .vgpr_spill_count: 0
    .wavefront_size: 64
